# g9: g8 + SSD z-gate epilogue regenerated stage by stage over the 16 elements
# speedup vs baseline: 1.0124x; 1.0002x over previous
.Lvmk_ssd_done:
	v_lshlrev_b32_e32 v75, 16, v6
	v_and_b32_e32 v125, 0xffff0000, v5
	v_lshl_add_u32 v74, s48, 7, v209
	s_waitcnt lgkmcnt(0)
	v_lshlrev_b32_e32 v68, 16, v66
	v_and_b32_e32 v66, 0xffff0000, v66
	v_lshlrev_b32_e32 v69, 16, v67
	v_and_b32_e32 v67, 0xffff0000, v67
	v_fma_f32 v66, v135, v66, v95
	v_fma_f32 v68, v135, v68, v94
	ds_write_b32 v204, v66 offset:272
	v_fma_f32 v66, v135, v69, v96
	v_fmac_f32_e32 v97, v135, v67
	ds_write_b32 v204, v68
	ds_write_b32 v204, v66 offset:544
	ds_write_b32 v204, v97 offset:816
	ds_read_b64 v[66:67], v188
	v_and_b32_e32 v94, 0xffff0000, v3
	v_lshlrev_b32_e32 v95, 16, v4
	v_and_b32_e32 v96, 0xffff0000, v4
	v_lshlrev_b32_e32 v97, 16, v5
	s_waitcnt lgkmcnt(0)
	v_lshlrev_b32_e32 v68, 16, v66
	v_and_b32_e32 v66, 0xffff0000, v66
	v_lshlrev_b32_e32 v69, 16, v67
	v_and_b32_e32 v67, 0xffff0000, v67
	v_fma_f32 v66, v135, v66, v91
	v_fma_f32 v68, v135, v68, v90
	ds_write_b32 v204, v66 offset:336
	v_fma_f32 v66, v135, v69, v92
	v_fmac_f32_e32 v93, v135, v67
	ds_write_b32 v204, v68 offset:64
	ds_write_b32 v204, v66 offset:608
	ds_write_b32 v204, v93 offset:880
	ds_read_b64 v[66:67], v189
	v_and_b32_e32 v90, 0xffff0000, v9
	v_lshlrev_b32_e32 v91, 16, v2
	v_and_b32_e32 v92, 0xffff0000, v2
	v_lshlrev_b32_e32 v93, 16, v3
	s_waitcnt lgkmcnt(0)
	v_lshlrev_b32_e32 v68, 16, v66
	v_and_b32_e32 v66, 0xffff0000, v66
	v_lshlrev_b32_e32 v69, 16, v67
	v_and_b32_e32 v67, 0xffff0000, v67
	v_fma_f32 v66, v135, v66, v87
	v_fma_f32 v68, v135, v68, v86
	ds_write_b32 v204, v66 offset:400
	v_fma_f32 v66, v135, v69, v88
	v_fmac_f32_e32 v89, v135, v67
	ds_write_b32 v204, v68 offset:128
	ds_write_b32 v204, v66 offset:672
	ds_write_b32 v204, v89 offset:944
	ds_read_b64 v[66:67], v190
	v_and_b32_e32 v86, 0xffff0000, v7
	v_lshlrev_b32_e32 v87, 16, v8
	v_and_b32_e32 v88, 0xffff0000, v8
	v_lshlrev_b32_e32 v89, 16, v9
	s_waitcnt lgkmcnt(0)
	v_lshlrev_b32_e32 v68, 16, v66
	v_and_b32_e32 v66, 0xffff0000, v66
	v_lshlrev_b32_e32 v69, 16, v67
	v_and_b32_e32 v67, 0xffff0000, v67
	v_fma_f32 v66, v135, v66, v83
	v_fma_f32 v68, v135, v68, v82
	ds_write_b32 v204, v66 offset:464
	v_fma_f32 v66, v135, v69, v84
	v_fmac_f32_e32 v85, v135, v67
	ds_write_b32 v204, v68 offset:192
	ds_write_b32 v204, v66 offset:736
	ds_write_b32 v204, v85 offset:1008
	ds_read_b128 v[76:79], v205
	ds_read_b128 v[80:83], v205 offset:16
	ds_read_b128 v[70:73], v205 offset:32
	ds_read_b128 v[66:69], v205 offset:48
	v_and_b32_e32 v84, 0xffff0000, v6
	v_lshlrev_b32_e32 v85, 16, v7
	s_waitcnt lgkmcnt(0)
	v_mul_f32_e32 v76, v76, v75
	v_mul_f32_e32 v77, v77, v84
	v_mul_f32_e32 v78, v78, v85
	v_mul_f32_e32 v79, v79, v86
	v_mul_f32_e32 v80, v80, v87
	v_mul_f32_e32 v81, v81, v88
	v_mul_f32_e32 v82, v82, v89
	v_mul_f32_e32 v83, v83, v90
	v_mul_f32_e32 v70, v70, v91
	v_mul_f32_e32 v71, v71, v92
	v_mul_f32_e32 v72, v72, v93
	v_mul_f32_e32 v73, v73, v94
	v_mul_f32_e32 v66, v66, v95
	v_mul_f32_e32 v67, v67, v96
	v_mul_f32_e32 v68, v68, v97
	v_mul_f32_e32 v69, v69, v125
	v_mul_f32_e32 v75, 0xbfb8aa3b, v75
	v_mul_f32_e32 v84, 0xbfb8aa3b, v84
	v_mul_f32_e32 v85, 0xbfb8aa3b, v85
	v_mul_f32_e32 v86, 0xbfb8aa3b, v86
	v_mul_f32_e32 v87, 0xbfb8aa3b, v87
	v_mul_f32_e32 v88, 0xbfb8aa3b, v88
	v_mul_f32_e32 v89, 0xbfb8aa3b, v89
	v_mul_f32_e32 v90, 0xbfb8aa3b, v90
	v_mul_f32_e32 v91, 0xbfb8aa3b, v91
	v_mul_f32_e32 v92, 0xbfb8aa3b, v92
	v_mul_f32_e32 v93, 0xbfb8aa3b, v93
	v_mul_f32_e32 v94, 0xbfb8aa3b, v94
	v_mul_f32_e32 v95, 0xbfb8aa3b, v95
	v_mul_f32_e32 v96, 0xbfb8aa3b, v96
	v_mul_f32_e32 v97, 0xbfb8aa3b, v97
	v_mul_f32_e32 v125, 0xbfb8aa3b, v125
	v_exp_f32_e32 v75, v75
	v_exp_f32_e32 v84, v84
	v_exp_f32_e32 v85, v85
	v_exp_f32_e32 v86, v86
	v_exp_f32_e32 v87, v87
	v_exp_f32_e32 v88, v88
	v_exp_f32_e32 v89, v89
	v_exp_f32_e32 v90, v90
	v_exp_f32_e32 v91, v91
	v_exp_f32_e32 v92, v92
	v_exp_f32_e32 v93, v93
	v_exp_f32_e32 v94, v94
	v_exp_f32_e32 v95, v95
	v_exp_f32_e32 v96, v96
	v_exp_f32_e32 v97, v97
	v_exp_f32_e32 v125, v125
	v_add_f32_e32 v75, 1.0, v75
	v_add_f32_e32 v84, 1.0, v84
	v_add_f32_e32 v85, 1.0, v85
	v_add_f32_e32 v86, 1.0, v86
	v_add_f32_e32 v87, 1.0, v87
	v_add_f32_e32 v88, 1.0, v88
	v_add_f32_e32 v89, 1.0, v89
	v_add_f32_e32 v90, 1.0, v90
	v_add_f32_e32 v91, 1.0, v91
	v_add_f32_e32 v92, 1.0, v92
	v_add_f32_e32 v93, 1.0, v93
	v_add_f32_e32 v94, 1.0, v94
	v_add_f32_e32 v95, 1.0, v95
	v_add_f32_e32 v96, 1.0, v96
	v_add_f32_e32 v97, 1.0, v97
	v_add_f32_e32 v125, 1.0, v125
	v_rcp_f32_e32 v75, v75
	v_rcp_f32_e32 v84, v84
	v_rcp_f32_e32 v85, v85
	v_rcp_f32_e32 v86, v86
	v_rcp_f32_e32 v87, v87
	v_rcp_f32_e32 v88, v88
	v_rcp_f32_e32 v89, v89
	v_rcp_f32_e32 v90, v90
	v_rcp_f32_e32 v91, v91
	v_rcp_f32_e32 v92, v92
	v_rcp_f32_e32 v93, v93
	v_rcp_f32_e32 v94, v94
	v_rcp_f32_e32 v95, v95
	v_rcp_f32_e32 v96, v96
	v_rcp_f32_e32 v97, v97
	v_rcp_f32_e32 v125, v125
	v_mul_f32_e32 v76, v75, v76
	v_mul_f32_e32 v77, v84, v77
	v_mul_f32_e32 v78, v85, v78
	v_mul_f32_e32 v79, v86, v79
	v_mul_f32_e32 v80, v87, v80
	v_mul_f32_e32 v81, v88, v81
	v_mul_f32_e32 v82, v89, v82
	v_mul_f32_e32 v83, v90, v83
	v_mul_f32_e32 v70, v91, v70
	v_mul_f32_e32 v71, v92, v71
	v_mul_f32_e32 v72, v93, v72
	v_mul_f32_e32 v73, v94, v73
	v_mul_f32_e32 v84, v95, v66
	v_mul_f32_e32 v85, v96, v67
	v_mul_f32_e32 v68, v97, v68
	v_mul_f32_e32 v69, v125, v69
	v_mul_f32_e32 v86, v77, v77
	v_fmac_f32_e32 v86, v76, v76
	v_fmac_f32_e32 v86, v78, v78
	v_fmac_f32_e32 v86, v79, v79
	v_fmac_f32_e32 v86, v80, v80
	v_fmac_f32_e32 v86, v81, v81
	v_fmac_f32_e32 v86, v82, v82
	v_fmac_f32_e32 v86, v83, v83
	v_fmac_f32_e32 v86, v70, v70
	v_fmac_f32_e32 v86, v71, v71
	v_fmac_f32_e32 v86, v72, v72
	v_fmac_f32_e32 v86, v73, v73
	v_fmac_f32_e32 v86, v84, v84
	v_fmac_f32_e32 v86, v85, v85
	v_fmac_f32_e32 v86, v68, v68
	v_ashrrev_i32_e32 v75, 31, v74
	v_xor_b32_e32 v87, 1, v99
	v_and_b32_e32 v66, 64, v99
	v_add_u32_e32 v67, 64, v66
	v_cmp_lt_i32_e32 vcc, v87, v67
	v_fmac_f32_e32 v86, v69, v69
	s_nop 0
	v_cndmask_b32_e32 v87, v99, v87, vcc
	v_lshlrev_b32_e32 v212, 2, v87
	ds_bpermute_b32 v87, v212, v86
	s_waitcnt lgkmcnt(0)
	v_add_f32_e32 v86, v86, v87
	v_xor_b32_e32 v87, 2, v99
	v_cmp_lt_i32_e32 vcc, v87, v67
	s_nop 1
	v_cndmask_b32_e32 v87, v99, v87, vcc
	v_lshlrev_b32_e32 v213, 2, v87
	ds_bpermute_b32 v87, v213, v86
	s_and_saveexec_b64 s[0:1], s[26:27]
	s_cbranch_execz .LBB0_234
	v_lshlrev_b64 v[88:89], 7, v[74:75]
	v_lshl_add_u64 v[88:89], s[38:39], 0, v[88:89]
	s_waitcnt lgkmcnt(0)
	v_add_f32_e32 v86, v86, v87
	global_store_dword v[88:89], v86, off
